# speedup vs baseline: 1.0135x; 1.0135x over previous
_Z11gemm_kernelILi128ELi192ELi1EEv8GemmArgs:
	s_load_dwordx2 s[4:5], s[0:1], 0x38
	s_load_dwordx2 s[22:23], s[0:1], 0x48
	s_load_dwordx2 s[24:25], s[0:1], 0x0
	s_load_dwordx2 s[26:27], s[0:1], 0x98
	s_addk_i32 s2, 0xe0
	s_mov_b32 s3, 0
	s_lshl_b64 s[6:7], s[2:3], 2
	s_waitcnt lgkmcnt(0)
	s_add_u32 s4, s4, s6
	s_addc_u32 s5, s5, s7
	s_load_dword s8, s[4:5], 0x0
	s_waitcnt lgkmcnt(0)
	s_cmp_lt_i32 s8, 0
	s_cbranch_scc1 .LBB3_4
	s_mov_b64 s[6:7], s[22:23]
	s_mov_b64 s[4:5], s[24:25]
	v_lshlrev_b32_e32 v64, 4, v0
	v_and_b32_e32 v1, 32, v0
	v_bitop3_b32 v1, v64, v1, 48 bitop3:0x6c
	s_and_b32 s2, s8, 0xffff
	v_bfe_u32 v4, v0, 2, 4
	v_lshrrev_b32_e32 v2, 1, v0
	v_lshrrev_b32_e32 v1, 1, v1
	v_lshrrev_b32_e32 v6, 3, v0
	v_and_or_b32 v1, v2, 32, v1
	v_add_u32_e32 v5, s2, v4
	v_and_b32_e32 v7, 48, v6
	s_movk_i32 s10, 0x70
	v_add_lshl_u32 v22, v5, v7, 12
	v_mov_b32_e32 v23, 0
	v_lshlrev_b32_e32 v44, 1, v1
	v_bitop3_b32 v1, v6, s10, 64 bitop3:0xc8
	s_waitcnt lgkmcnt(0)
	v_lshl_add_u64 v[2:3], s[4:5], 0, v[22:23]
	v_mov_b32_e32 v45, v23
	v_add_lshl_u32 v48, v5, v1, 12
	v_mov_b32_e32 v49, v23
	s_lshr_b32 s10, s8, 24
	s_bfe_u32 s9, s8, 0x80010
	v_lshl_add_u64 v[46:47], v[2:3], 0, v[44:45]
	v_lshl_add_u64 v[2:3], s[4:5], 0, v[48:49]
	s_mulk_i32 s10, 0x300
	v_lshl_add_u64 v[50:51], v[2:3], 0, v[44:45]
	s_mul_i32 s8, s9, 0xc0
	v_or_b32_e32 v2, s10, v4
	v_add_u32_e32 v4, s8, v2
	v_or_b32_e32 v2, v4, v7
	v_lshlrev_b32_e32 v52, 12, v2
	v_mov_b32_e32 v53, v23
	v_lshl_add_u64 v[2:3], s[6:7], 0, v[52:53]
	v_add_lshl_u32 v56, v4, v1, 12
	v_mov_b32_e32 v57, v23
	v_lshl_add_u64 v[54:55], v[2:3], 0, v[44:45]
	v_lshl_add_u64 v[2:3], s[6:7], 0, v[56:57]
	v_add_u32_e32 v60, 0x80000, v52
	v_mov_b32_e32 v61, v23
	v_lshl_add_u64 v[58:59], v[2:3], 0, v[44:45]
	v_lshl_add_u64 v[2:3], s[6:7], 0, v[60:61]
	v_lshl_add_u64 v[62:63], v[2:3], 0, v[44:45]
	v_readfirstlane_b32 s16, v0
	s_mov_b64 s[0:1], s[26:27]
	s_lshr_b32 s16, s16, 6
	s_lshl_b32 s16, s16, 10
	v_bfe_u32 v1, v0, 6, 2
	v_lshrrev_b32_e32 v80, 2, v0
	s_add_u32 m0, s16, 0
	s_nop 0
	global_load_lds_dwordx4 v[46:47], off
	s_add_u32 m0, s16, 8192
	s_nop 0
	global_load_lds_dwordx4 v[50:51], off
	s_add_u32 m0, s16, 16384
	s_nop 0
	global_load_lds_dwordx4 v[54:55], off
	s_add_u32 m0, s16, 24576
	s_nop 0
	global_load_lds_dwordx4 v[58:59], off
	s_add_u32 m0, s16, 32768
	s_nop 0
	global_load_lds_dwordx4 v[62:63], off
	s_add_u32 m0, s16, 40832
	s_nop 0
	global_load_lds_dwordx4 v[46:47], off offset:128
	s_add_u32 m0, s16, 49024
	s_nop 0
	global_load_lds_dwordx4 v[50:51], off offset:128
	s_add_u32 m0, s16, 57216
	s_nop 0
	global_load_lds_dwordx4 v[54:55], off offset:128
	s_add_u32 m0, s16, 65408
	s_nop 0
	global_load_lds_dwordx4 v[58:59], off offset:128
	s_add_u32 m0, s16, 73600
	s_nop 0
	global_load_lds_dwordx4 v[62:63], off offset:128
	s_mov_b32 s17, 0
	s_mov_b32 s18, 0xa000
	s_mov_b32 s19, 0x14000
	v_lshlrev_b32_e32 v25, 6, v0
	v_lshlrev_b32_e32 v27, 2, v0
	v_and_b32_e32 v24, 48, v0
	v_and_b32_e32 v25, 0x3c0, v25
	v_and_b32_e32 v27, 32, v27
	v_or_b32_e32 v26, v25, v24
	v_bitop3_b32 v87, v25, v27, v24 bitop3:0x36
	v_or_b32_e32 v24, v44, v60
	v_mov_b32_e32 v25, v23
	v_lshl_add_u64 v[24:25], s[6:7], 0, v[24:25]
	s_mov_b64 s[10:11], 0x100
	v_lshl_add_u64 v[70:71], v[24:25], 0, s[10:11]
	v_or_b32_e32 v24, v56, v44
	v_mov_b32_e32 v25, v23
	v_lshl_add_u64 v[24:25], s[6:7], 0, v[24:25]
	v_lshl_add_u64 v[72:73], v[24:25], 0, s[10:11]
	v_or_b32_e32 v24, v52, v44
	v_mov_b32_e32 v25, v23
	v_lshl_add_u64 v[24:25], s[6:7], 0, v[24:25]
	v_lshl_add_u64 v[74:75], v[24:25], 0, s[10:11]
	v_or_b32_e32 v24, v48, v44
	v_mov_b32_e32 v25, v23
	v_lshl_add_u64 v[24:25], s[4:5], 0, v[24:25]
	v_or_b32_e32 v22, v22, v44
	v_and_b32_e32 v81, 64, v80
	v_mul_u32_u24_e32 v86, 0x1800, v1
	v_lshl_add_u64 v[76:77], v[24:25], 0, s[10:11]
	v_lshl_add_u64 v[24:25], s[4:5], 0, v[22:23]
	v_bitop3_b32 v82, v26, v86, v27 bitop3:0xde
	v_lshlrev_b32_e32 v88, 7, v81
	v_lshl_add_u64 v[78:79], v[24:25], 0, s[10:11]
	s_mov_b64 s[4:5], 0
	v_mov_b32_e32 v22, v23
	v_mov_b32_e32 v24, v23
	v_mov_b32_e32 v25, v23
	v_mov_b32_e32 v50, v23
	v_mov_b32_e32 v51, v23
	v_mov_b32_e32 v52, v23
	v_mov_b32_e32 v54, v23
	v_mov_b32_e32 v55, v23
	v_mov_b32_e32 v56, v23
	v_mov_b32_e32 v58, v23
	v_mov_b32_e32 v59, v23
	v_mov_b32_e32 v60, v23
	v_mov_b32_e32 v66, v23
	v_mov_b32_e32 v67, v23
	v_mov_b32_e32 v68, v23
	v_mov_b32_e32 v69, v23
	v_mov_b32_e32 v62, v23
	v_mov_b32_e32 v63, v23
	v_mov_b32_e32 v64, v23
	v_mov_b32_e32 v65, v23
	v_mov_b32_e32 v42, v23
	v_mov_b32_e32 v43, v23
	v_mov_b32_e32 v44, v23
	v_mov_b32_e32 v46, v23
	v_mov_b32_e32 v47, v23
	v_mov_b32_e32 v48, v23
	v_mov_b32_e32 v30, v23
	v_mov_b32_e32 v31, v23
	v_mov_b32_e32 v32, v23
	v_mov_b32_e32 v33, v23
	v_mov_b32_e32 v34, v23
	v_mov_b32_e32 v35, v23
	v_mov_b32_e32 v36, v23
	v_mov_b32_e32 v37, v23
	v_mov_b32_e32 v38, v23
	v_mov_b32_e32 v39, v23
	v_mov_b32_e32 v40, v23
	v_mov_b32_e32 v41, v23
	v_mov_b32_e32 v26, v23
	v_mov_b32_e32 v27, v23
	v_mov_b32_e32 v28, v23
	v_mov_b32_e32 v29, v23
	s_waitcnt vmcnt(5) lgkmcnt(0)
	s_barrier
	s_nop 0
	s_nop 0
	s_nop 0
